# LRU loop: scan passes preload 32 LDS values once (pass2 reuses regs), gelu output stage rewritten with packed f32 + folded constants
# speedup vs baseline: 1.0209x; 1.0023x over previous
; #define LAS __attribute__((address_space(3)))
; __device__ __forceinline__ unsigned pk2(float lo, float hi) { const f32x2c_t v = {lo, hi}; const bf16x2c_t b = __builtin_convertvector(v, bf16x2c_t); return __builtin_bit_cast(unsigned, b); }
; __device__ __forceinline__ float bflo(unsigned w) { return __uint_as_float(w << 16); }
; __device__ __forceinline__ float bfhi(unsigned w) { return __uint_as_float(w & 0xffff0000u); }
; __device__ __forceinline__ f32x4 mfma16(bf16x8 a, bf16x8 b, f32x4 c) { return __builtin_amdgcn_mfma_f32_16x16x32_bf16(a, b, c, 0, 0, 0); }
; template <int MODE> ...
;     ...
;         if (unit + G < NCH * 8) issue(unit + G);
;         QRow qrow; const int qe = unit * 8 + wid;
;         if (QUANT_IN_LRU) quant_issue(qrow, MODE == 1 ? P.peer_v : P.peer_u, qe, lane);
; #pragma unroll
;         for (int rr = 0; rr < 8; ++rr) {
;             float x0 = cb0, x1 = cb1;
; #pragma unroll
;             for (int kk = 0; kk < 4; ++kk) { x0 += cw0[kk] * bflo(xcur[rr + kk]); x1 += cw1[kk] * bfhi(xcur[rr + kk]); }
;             const int row = wid * 8 + rr;
;             XC[row * 132 + 2 * lane] = x0; XC[row * 132 + 2 * lane + 1] = x1;
;             *(LAS unsigned*)(XCb + row * 136 + 2 * lane) = pk2(x0, x1);
;         }
;         __syncthreads();
;         {
;             f32x4 ar[4], ai[4];
; #pragma unroll
;             for (int j = 0; j < 4; ++j) { ar[j] = (f32x4){0.f, 0.f, 0.f, 0.f}; ai[j] = (f32x4){0.f, 0.f, 0.f, 0.f}; }
; #pragma unroll
;             for (int ks = 0; ks < 4; ++ks) {
;                 const bf16x8 a = *(const LAS bf16x8*)(XCb + (st * 16 + fr) * 136 + ks * 32 + fq * 8);
; #pragma unroll
;                 for (int j = 0; j < 4; ++j) { const int wo = ((jt0 + j) * 16 + fr) * 136 + ks * 32 + fq * 8;
;                     ar[j] = mfma16(a, *(const LAS bf16x8*)(WR + wo), ar[j]); ai[j] = mfma16(a, *(const LAS bf16x8*)(WI + wo), ai[j]); }
.LBB0_261:
	s_add_i32 s48, s53, s17
	s_ashr_i32 s49, s48, 31
	v_lshlrev_b32_e32 v62, 16, v51
	v_and_b32_e32 v63, 0xffff0000, v51
	s_lshl_b64 s[6:7], s[48:49], 13
	v_lshlrev_b32_e32 v64, 16, v50
	v_and_b32_e32 v65, 0xffff0000, v50
	v_pk_fma_f32 v[62:63], v[102:103], v[62:63], v[104:105]
	v_lshl_add_u64 v[18:19], v[86:87], 0, s[6:7]
	v_lshlrev_b32_e32 v50, 16, v52
	v_and_b32_e32 v51, 0xffff0000, v52
	v_pk_fma_f32 v[62:63], v[98:99], v[64:65], v[62:63]
	global_load_dwordx4 v[46:49], v[18:19], off nt
	global_load_dwordx4 v[42:45], v[18:19], off offset:1024 nt
	global_load_dwordx4 v[38:41], v[18:19], off offset:2048 nt
	global_load_dwordx4 v[34:37], v[18:19], off offset:3072 nt
	v_add_co_u32_e32 v18, vcc, 0x1000, v18
	v_lshlrev_b32_e32 v52, 16, v53
	v_and_b32_e32 v53, 0xffff0000, v53
	v_pk_fma_f32 v[62:63], v[96:97], v[50:51], v[62:63]
	s_mul_i32 s0, s53, 0x1080
	v_addc_co_u32_e32 v19, vcc, 0, v19, vcc
	v_pk_fma_f32 v[62:63], v[100:101], v[52:53], v[62:63]
	v_add_u32_e32 v61, s0, v83
	s_mul_i32 s0, s53, 0x880
	v_pk_fma_f32 v[64:65], v[102:103], v[64:65], v[104:105]
	global_load_dwordx4 v[30:33], v[18:19], off nt
	global_load_dwordx4 v[26:29], v[18:19], off offset:1024 nt
	global_load_dwordx4 v[22:25], v[18:19], off offset:2048 nt
	s_nop 0
	global_load_dwordx4 v[18:21], v[18:19], off offset:3072 nt
	ds_write_b64 v61, v[62:63]
	v_cvt_pk_bf16_f32 v61, v62, v63
	v_add_u32_e32 v62, s0, v110
	v_pk_fma_f32 v[64:65], v[98:99], v[50:51], v[64:65]
	v_pk_fma_f32 v[50:51], v[102:103], v[50:51], v[104:105]
	ds_write_b32 v62, v61 offset:33792
	v_lshlrev_b32_e32 v62, 16, v55
	v_and_b32_e32 v63, 0xffff0000, v55
	v_pk_fma_f32 v[50:51], v[98:99], v[52:53], v[50:51]
	v_pk_fma_f32 v[64:65], v[96:97], v[52:53], v[64:65]
	v_lshlrev_b32_e32 v66, 16, v56
	v_and_b32_e32 v67, 0xffff0000, v56
	v_pk_fma_f32 v[50:51], v[96:97], v[62:63], v[50:51]
	v_pk_fma_f32 v[64:65], v[100:101], v[62:63], v[64:65]
	v_add_u32_e32 v61, s37, v83
	v_add_u32_e32 v68, s85, v110
	v_pk_fma_f32 v[50:51], v[100:101], v[66:67], v[50:51]
	v_cvt_pk_bf16_f32 v55, v64, v65
	ds_write2_b64 v61, v[64:65], v[50:51] offset1:66
	v_cvt_pk_bf16_f32 v50, v50, v51
	v_add_u32_e32 v64, 0x8400, v68
	ds_write2_b32 v64, v55, v50 offset1:68
	v_lshlrev_b32_e32 v50, 16, v57
	v_and_b32_e32 v51, 0xffff0000, v57
	v_pk_fma_f32 v[52:53], v[102:103], v[52:53], v[104:105]
	v_lshlrev_b32_e32 v56, 16, v54
	v_and_b32_e32 v57, 0xffff0000, v54
	v_pk_fma_f32 v[54:55], v[102:103], v[62:63], v[104:105]
	v_pk_fma_f32 v[52:53], v[98:99], v[62:63], v[52:53]
	v_pk_fma_f32 v[54:55], v[98:99], v[66:67], v[54:55]
	v_pk_fma_f32 v[52:53], v[96:97], v[66:67], v[52:53]
	v_pk_fma_f32 v[54:55], v[96:97], v[50:51], v[54:55]
	v_pk_fma_f32 v[52:53], v[100:101], v[50:51], v[52:53]
	v_pk_fma_f32 v[54:55], v[100:101], v[56:57], v[54:55]
	v_cvt_pk_bf16_f32 v65, v52, v53
	ds_write2_b64 v61, v[52:53], v[54:55] offset0:132 offset1:198
	v_cvt_pk_bf16_f32 v52, v54, v55
	v_pk_fma_f32 v[54:55], v[102:103], v[66:67], v[104:105]
	ds_write2_b32 v64, v65, v52 offset0:136 offset1:204
	v_pk_fma_f32 v[54:55], v[98:99], v[50:51], v[54:55]
	v_pk_fma_f32 v[50:51], v[102:103], v[50:51], v[104:105]
	v_lshlrev_b32_e32 v52, 16, v58
	v_and_b32_e32 v53, 0xffff0000, v58
	v_pk_fma_f32 v[50:51], v[98:99], v[56:57], v[50:51]
	v_pk_fma_f32 v[54:55], v[96:97], v[56:57], v[54:55]
	v_lshlrev_b32_e32 v58, 16, v59
	v_and_b32_e32 v59, 0xffff0000, v59
	v_pk_fma_f32 v[50:51], v[96:97], v[52:53], v[50:51]
	v_pk_fma_f32 v[54:55], v[100:101], v[52:53], v[54:55]
	v_pk_fma_f32 v[50:51], v[100:101], v[58:59], v[50:51]
	v_add_u32_e32 v63, 0x800, v61
	v_cvt_pk_bf16_f32 v62, v54, v55
	ds_write2_b64 v63, v[54:55], v[50:51] offset0:8 offset1:74
	v_pk_fma_f32 v[54:55], v[102:103], v[56:57], v[104:105]
	v_cvt_pk_bf16_f32 v50, v50, v51
	v_add_u32_e32 v51, 0x8800, v68
	v_pk_fma_f32 v[52:53], v[98:99], v[52:53], v[54:55]
	ds_write2_b32 v51, v62, v50 offset0:16 offset1:84
	v_lshlrev_b32_e32 v50, 16, v60
	v_and_b32_e32 v51, 0xffff0000, v60
	v_pk_fma_f32 v[52:53], v[96:97], v[58:59], v[52:53]
	s_nop 0
	v_pk_fma_f32 v[50:51], v[100:101], v[50:51], v[52:53]
	ds_write_b64 v61, v[50:51] offset:3168
	v_cvt_pk_bf16_f32 v50, v50, v51
	ds_write_b32 v68, v50 offset:35424
	s_waitcnt lgkmcnt(0)
	s_barrier
	ds_read_b128 v[50:53], v111 offset:33792
	ds_read_b128 v[54:57], v122
	ds_read_b128 v[58:61], v123
	ds_read_b128 v[62:65], v124
	ds_read_b128 v[66:69], v125
	ds_read_b128 v[70:73], v126
	ds_read_b128 v[74:77], v127
	ds_read_b128 v[190:193], v128
	ds_read_b128 v[194:197], v129
	s_waitcnt lgkmcnt(7)
	v_mfma_f32_16x16x32_bf16 v[54:57], v[50:53], v[54:57], 0
	s_waitcnt lgkmcnt(6)
	v_mfma_f32_16x16x32_bf16 v[58:61], v[50:53], v[58:61], 0
	s_waitcnt lgkmcnt(5)
	v_mfma_f32_16x16x32_bf16 v[62:65], v[50:53], v[62:65], 0
	s_waitcnt lgkmcnt(4)
	v_mfma_f32_16x16x32_bf16 v[66:69], v[50:53], v[66:69], 0
	s_waitcnt lgkmcnt(3)
	v_mfma_f32_16x16x32_bf16 v[70:73], v[50:53], v[70:73], 0
	s_waitcnt lgkmcnt(2)
	v_mfma_f32_16x16x32_bf16 v[74:77], v[50:53], v[74:77], 0
	s_waitcnt lgkmcnt(1)
	v_mfma_f32_16x16x32_bf16 v[190:193], v[50:53], v[190:193], 0
	s_waitcnt lgkmcnt(0)
	v_mfma_f32_16x16x32_bf16 v[50:53], v[50:53], v[194:197], 0
	ds_read_b128 v[194:197], v111 offset:33856
	ds_read_b128 v[198:201], v130
	s_waitcnt lgkmcnt(0)
	v_mfma_f32_16x16x32_bf16 v[54:57], v[194:197], v[198:201], v[54:57]
	ds_read_b128 v[198:201], v131
	s_waitcnt lgkmcnt(0)
	v_mfma_f32_16x16x32_bf16 v[58:61], v[194:197], v[198:201], v[58:61]
	ds_read_b128 v[198:201], v132
	s_waitcnt lgkmcnt(0)
	v_mfma_f32_16x16x32_bf16 v[62:65], v[194:197], v[198:201], v[62:65]
	ds_read_b128 v[198:201], v133
	s_waitcnt lgkmcnt(0)
; #define LAS __attribute__((address_space(3)))
; __device__ __forceinline__ f32x4 mfma16(bf16x8 a, bf16x8 b, f32x4 c) { return __builtin_amdgcn_mfma_f32_16x16x32_bf16(a, b, c, 0, 0, 0); }
; __device__ __forceinline__ float fexp_(float x) { return __builtin_amdgcn_exp2f(x * 1.4426950408889634f); }
; __device__ __forceinline__ float sigmoidf_(float x) { return __builtin_amdgcn_rcpf(1.0f + fexp_(-x)); }
; template <int MODE> ...
;     ...
; #pragma unroll
;             for (int ks = 0; ks < 4; ++ks) {
;                 const bf16x8 a = *(const LAS bf16x8*)(XCb + (st * 16 + fr) * 136 + ks * 32 + fq * 8);
; #pragma unroll
;                 for (int j = 0; j < 4; ++j) { const int wo = ((jt0 + j) * 16 + fr) * 136 + ks * 32 + fq * 8;
;                     ar[j] = mfma16(a, *(const LAS bf16x8*)(WR + wo), ar[j]); ai[j] = mfma16(a, *(const LAS bf16x8*)(WI + wo), ai[j]); }
;             }
; #pragma unroll
;             for (int j = 0; j < 4; ++j) {
;                 const int col = (jt0 + j) * 16 + fr;
; #pragma unroll
;                 for (int r = 0; r < 4; ++r) {
;                     const int sl = st * 16 + fq * 4 + r;
;                     const float rg = sigmoidf_(ar[j][r] + bra[j]), ig = sigmoidf_(ai[j][r] + bri[j]);
;                     const float a = fexp_(rg * ls[j]);
;                     const float bv = __builtin_amdgcn_sqrtf(fmaxf(1.0f - a * a, 0.f)) * (ig * XC[sl * 132 + col]);
;                     AA[sl * 132 + col] = a; BB[sl * 132 + col] = bv;
;                 }
;             }
	v_mfma_f32_16x16x32_bf16 v[66:69], v[194:197], v[198:201], v[66:69]
	ds_read_b128 v[198:201], v134
	s_waitcnt lgkmcnt(0)
	v_mfma_f32_16x16x32_bf16 v[70:73], v[194:197], v[198:201], v[70:73]
	ds_read_b128 v[198:201], v135
	s_waitcnt lgkmcnt(0)
	v_mfma_f32_16x16x32_bf16 v[74:77], v[194:197], v[198:201], v[74:77]
	ds_read_b128 v[198:201], v136
	s_waitcnt lgkmcnt(0)
	v_mfma_f32_16x16x32_bf16 v[190:193], v[194:197], v[198:201], v[190:193]
	ds_read_b128 v[198:201], v137
	s_waitcnt lgkmcnt(0)
	v_mfma_f32_16x16x32_bf16 v[50:53], v[194:197], v[198:201], v[50:53]
	ds_read_b128 v[194:197], v111 offset:33920
	ds_read_b128 v[198:201], v138
	s_waitcnt lgkmcnt(0)
	v_mfma_f32_16x16x32_bf16 v[54:57], v[194:197], v[198:201], v[54:57]
	ds_read_b128 v[198:201], v139
	s_waitcnt lgkmcnt(0)
	v_mfma_f32_16x16x32_bf16 v[58:61], v[194:197], v[198:201], v[58:61]
	ds_read_b128 v[198:201], v140
	s_waitcnt lgkmcnt(0)
	v_mfma_f32_16x16x32_bf16 v[62:65], v[194:197], v[198:201], v[62:65]
	ds_read_b128 v[198:201], v141
	s_waitcnt lgkmcnt(0)
	v_mfma_f32_16x16x32_bf16 v[66:69], v[194:197], v[198:201], v[66:69]
	ds_read_b128 v[198:201], v142
	s_waitcnt lgkmcnt(0)
	v_mfma_f32_16x16x32_bf16 v[198:201], v[194:197], v[198:201], v[70:73]
	s_nop 2
	ds_read_b128 v[70:73], v143
	s_waitcnt lgkmcnt(0)
	v_mfma_f32_16x16x32_bf16 v[214:217], v[194:197], v[70:73], v[74:77]
	ds_read_b128 v[70:73], v144
	s_waitcnt lgkmcnt(0)
	v_mfma_f32_16x16x32_bf16 v[190:193], v[194:197], v[70:73], v[190:193]
	ds_read_b128 v[70:73], v145
	s_waitcnt lgkmcnt(0)
	v_mfma_f32_16x16x32_bf16 v[50:53], v[194:197], v[70:73], v[50:53]
	ds_read_b128 v[194:197], v111 offset:33984
	ds_read_b128 v[70:73], v146
	s_waitcnt lgkmcnt(0)
	v_mfma_f32_16x16x32_bf16 v[218:221], v[194:197], v[70:73], v[54:57]
	s_nop 2
	ds_read_b128 v[54:57], v147
	s_waitcnt lgkmcnt(0)
	v_mfma_f32_16x16x32_bf16 v[74:77], v[194:197], v[54:57], v[58:61]
	s_nop 1
	v_add_f32_e32 v84, v167, v218
	v_mul_f32_e32 v84, 0xbfb8aa3b, v84
	v_exp_f32_e32 v84, v84
	ds_read_b128 v[54:57], v148
	s_waitcnt lgkmcnt(0)
	v_mfma_f32_16x16x32_bf16 v[70:73], v[194:197], v[54:57], v[62:65]
	v_add_f32_e32 v84, 1.0, v84
	v_rcp_f32_e32 v84, v84
	ds_read_b128 v[54:57], v149
	v_add_f32_e32 v74, v173, v74
	v_mul_f32_e32 v74, 0xbfb8aa3b, v74
	v_mul_f32_e32 v84, v94, v84
	v_mul_f32_e32 v84, 0x3fb8aa3b, v84
	v_exp_f32_e32 v84, v84
	v_exp_f32_e32 v74, v74
	s_waitcnt lgkmcnt(0)
	v_mfma_f32_16x16x32_bf16 v[66:69], v[194:197], v[54:57], v[66:69]
	ds_read_b128 v[54:57], v150
	v_fma_f32 v108, -v84, v84, 1.0
	v_max_f32_e32 v108, 0, v108
	v_add_f32_e32 v74, 1.0, v74
	v_sqrt_f32_e32 v189, v108
	ds_read2_b32 v[108:109], v154 offset1:16
	v_rcp_f32_e32 v74, v74
	s_waitcnt lgkmcnt(1)
	v_mfma_f32_16x16x32_bf16 v[62:65], v[194:197], v[54:57], v[198:201]
	ds_read_b128 v[54:57], v151
	v_add_f32_e32 v75, v173, v75
	s_waitcnt lgkmcnt(1)
	v_mul_f32_e32 v74, v74, v108
	v_mul_f32_e32 v108, v189, v74
	v_add_f32_e32 v74, v167, v219
	v_mul_f32_e32 v74, 0xbfb8aa3b, v74
	v_exp_f32_e32 v74, v74
	s_waitcnt lgkmcnt(0)
	v_mfma_f32_16x16x32_bf16 v[58:61], v[194:197], v[54:57], v[214:217]
	ds_read_b128 v[54:57], v152
	v_mul_f32_e32 v75, 0xbfb8aa3b, v75
	v_add_f32_e32 v74, 1.0, v74
	v_rcp_f32_e32 v74, v74
	s_waitcnt lgkmcnt(0)
	v_mfma_f32_16x16x32_bf16 v[54:57], v[194:197], v[54:57], v[190:193]
	v_exp_f32_e32 v75, v75
	v_mul_f32_e32 v74, v94, v74
	s_nop 0
	ds_read_b128 v[190:193], v153
	v_mul_f32_e32 v74, 0x3fb8aa3b, v74
	s_waitcnt lgkmcnt(0)
	v_mfma_f32_16x16x32_bf16 v[50:53], v[194:197], v[190:193], v[50:53]
	v_exp_f32_e32 v190, v74
	v_add_f32_e32 v75, 1.0, v75
	v_add_u32_e32 v192, 0x200, v154
	v_rcp_f32_e32 v189, v75
	v_fma_f32 v74, -v190, v190, 1.0
	v_max_f32_e32 v74, 0, v74
	v_sqrt_f32_e32 v191, v74
	ds_read2_b32 v[74:75], v192 offset0:4 offset1:136
	v_add_f32_e32 v76, v173, v76
	v_mul_f32_e32 v76, 0xbfb8aa3b, v76
	v_exp_f32_e32 v76, v76
	v_add_f32_e32 v70, v169, v70
	s_waitcnt lgkmcnt(0)
	v_mul_f32_e32 v74, v189, v74
	v_add_f32_e32 v189, v167, v220
	v_mul_f32_e32 v189, 0xbfb8aa3b, v189
	v_exp_f32_e32 v189, v189
	v_mul_f32_e32 v74, v191, v74
	v_add_f32_e32 v76, 1.0, v76
	v_rcp_f32_e32 v76, v76
	v_add_f32_e32 v189, 1.0, v189
	v_rcp_f32_e32 v189, v189
	v_mul_f32_e32 v70, 0xbfb8aa3b, v70
	v_mul_f32_e32 v75, v76, v75
	v_add_u32_e32 v76, 0xca00, v154
	v_mul_f32_e32 v189, v94, v189
	v_mul_f32_e32 v189, 0x3fb8aa3b, v189
	v_exp_f32_e32 v189, v189
	v_exp_f32_e32 v70, v70
	v_add_f32_e32 v66, v174, v66
	v_mul_f32_e32 v66, 0xbfb8aa3b, v66
	v_fma_f32 v191, -v189, v189, 1.0
	v_max_f32_e32 v191, 0, v191
	v_sqrt_f32_e32 v191, v191
	v_add_f32_e32 v70, 1.0, v70
	v_rcp_f32_e32 v70, v70
	v_exp_f32_e32 v66, v66
	v_mul_f32_e32 v75, v191, v75
	ds_write2_b32 v76, v190, v189 offset0:4 offset1:136
	ds_write2_b32 v192, v74, v75 offset0:4 offset1:136
	v_add_f32_e32 v74, v167, v221
	v_mul_f32_e32 v74, 0xbfb8aa3b, v74
	v_exp_f32_e32 v74, v74
	v_add_f32_e32 v75, v173, v77
	v_mul_f32_e32 v75, 0xbfb8aa3b, v75
	v_exp_f32_e32 v75, v75
	v_add_f32_e32 v74, 1.0, v74
	v_rcp_f32_e32 v74, v74
	ds_read_b32 v77, v154 offset:1584
	v_add_f32_e32 v75, 1.0, v75
	v_mul_f32_e32 v70, v95, v70
	v_mul_f32_e32 v74, v94, v74
	v_mul_f32_e32 v74, 0x3fb8aa3b, v74
	v_exp_f32_e32 v74, v74
	v_rcp_f32_e32 v75, v75
	v_mul_f32_e32 v70, 0x3fb8aa3b, v70
	v_exp_f32_e32 v70, v70
	v_fma_f32 v76, -v74, v74, 1.0
	v_max_f32_e32 v76, 0, v76
	v_sqrt_f32_e32 v76, v76
	s_waitcnt lgkmcnt(0)
; __device__ __forceinline__ float fexp_(float x) { return __builtin_amdgcn_exp2f(x * 1.4426950408889634f); }
; __device__ __forceinline__ float sigmoidf_(float x) { return __builtin_amdgcn_rcpf(1.0f + fexp_(-x)); }
; template <int MODE> ...
;     ...
;             for (int j = 0; j < 4; ++j) {
;                 const int col = (jt0 + j) * 16 + fr;
; #pragma unroll
;                 for (int r = 0; r < 4; ++r) {
;                     const int sl = st * 16 + fq * 4 + r;
;                     const float rg = sigmoidf_(ar[j][r] + bra[j]), ig = sigmoidf_(ai[j][r] + bri[j]);
;                     const float a = fexp_(rg * ls[j]);
;                     const float bv = __builtin_amdgcn_sqrtf(fmaxf(1.0f - a * a, 0.f)) * (ig * XC[sl * 132 + col]);
;                     AA[sl * 132 + col] = a; BB[sl * 132 + col] = bv;
;                 }
;             }
	v_mul_f32_e32 v75, v75, v77
	v_add_f32_e32 v66, 1.0, v66
	v_rcp_f32_e32 v66, v66
	v_mul_f32_e32 v75, v76, v75
	ds_write_b32 v154, v74 offset:52784
	ds_write_b32 v154, v75 offset:1584
	v_fma_f32 v74, -v70, v70, 1.0
	v_max_f32_e32 v74, 0, v74
	v_sqrt_f32_e32 v74, v74
	v_mul_f32_e32 v66, v66, v109
	v_add_f32_e32 v67, v174, v67
	v_mul_f32_e32 v67, 0xbfb8aa3b, v67
	v_mul_f32_e32 v66, v74, v66
	v_add_u32_e32 v74, 0xc800, v154
	ds_write2_b32 v74, v84, v70 offset1:16
	ds_write2_b32 v154, v108, v66 offset1:16
	v_add_f32_e32 v66, v169, v71
	v_mul_f32_e32 v66, 0xbfb8aa3b, v66
	v_exp_f32_e32 v66, v66
	v_exp_f32_e32 v67, v67
	v_add_u32_e32 v75, 0x200, v155
	v_add_f32_e32 v68, v174, v68
	v_add_f32_e32 v66, 1.0, v66
	v_rcp_f32_e32 v66, v66
	v_add_f32_e32 v67, 1.0, v67
	v_rcp_f32_e32 v70, v67
	v_mul_f32_e32 v68, 0xbfb8aa3b, v68
	v_mul_f32_e32 v66, v95, v66
	v_mul_f32_e32 v66, 0x3fb8aa3b, v66
	v_exp_f32_e32 v71, v66
	v_exp_f32_e32 v68, v68
	v_add_f32_e32 v62, v171, v62
	v_mul_f32_e32 v62, 0xbfb8aa3b, v62
	v_fma_f32 v66, -v71, v71, 1.0
	v_max_f32_e32 v66, 0, v66
	v_sqrt_f32_e32 v74, v66
	ds_read2_b32 v[66:67], v75 offset0:4 offset1:136
	v_add_f32_e32 v68, 1.0, v68
	v_rcp_f32_e32 v68, v68
	v_exp_f32_e32 v62, v62
	v_add_f32_e32 v58, v175, v58
	s_waitcnt lgkmcnt(0)
	v_mul_f32_e32 v66, v70, v66
	v_add_f32_e32 v70, v169, v72
	v_mul_f32_e32 v70, 0xbfb8aa3b, v70
	v_exp_f32_e32 v70, v70
	v_mul_f32_e32 v66, v74, v66
	v_mul_f32_e32 v67, v68, v67
	v_add_u32_e32 v68, 0xca00, v155
	v_add_f32_e32 v70, 1.0, v70
	v_rcp_f32_e32 v70, v70
	v_add_f32_e32 v62, 1.0, v62
	v_rcp_f32_e32 v62, v62
	v_mul_f32_e32 v58, 0xbfb8aa3b, v58
	v_mul_f32_e32 v70, v95, v70
	v_mul_f32_e32 v70, 0x3fb8aa3b, v70
	v_exp_f32_e32 v70, v70
	v_mul_f32_e32 v62, v106, v62
	v_mul_f32_e32 v62, 0x3fb8aa3b, v62
	v_exp_f32_e32 v58, v58
	v_fma_f32 v72, -v70, v70, 1.0
	v_max_f32_e32 v72, 0, v72
	v_sqrt_f32_e32 v72, v72
	v_exp_f32_e32 v62, v62
	v_add_f32_e32 v58, 1.0, v58
	v_rcp_f32_e32 v58, v58
	v_mul_f32_e32 v67, v72, v67
	ds_write2_b32 v68, v71, v70 offset0:4 offset1:136
	ds_write2_b32 v75, v66, v67 offset0:4 offset1:136
	v_add_f32_e32 v66, v169, v73
	v_mul_f32_e32 v66, 0xbfb8aa3b, v66
	v_exp_f32_e32 v66, v66
	v_add_f32_e32 v67, v174, v69
	v_mul_f32_e32 v67, 0xbfb8aa3b, v67
	v_exp_f32_e32 v67, v67
	v_add_f32_e32 v66, 1.0, v66
	v_rcp_f32_e32 v66, v66
	ds_read_b32 v69, v155 offset:1584
	v_add_f32_e32 v67, 1.0, v67
	v_rcp_f32_e32 v67, v67
	v_mul_f32_e32 v66, v95, v66
	v_mul_f32_e32 v66, 0x3fb8aa3b, v66
	v_exp_f32_e32 v66, v66
	s_waitcnt lgkmcnt(0)
	v_mul_f32_e32 v67, v67, v69
	v_add_f32_e32 v59, v175, v59
	v_mul_f32_e32 v59, 0xbfb8aa3b, v59
	v_fma_f32 v68, -v66, v66, 1.0
	v_max_f32_e32 v68, 0, v68
	v_sqrt_f32_e32 v68, v68
	v_exp_f32_e32 v59, v59
	v_add_f32_e32 v60, v175, v60
	v_mul_f32_e32 v60, 0xbfb8aa3b, v60
	v_mul_f32_e32 v67, v68, v67
	ds_write_b32 v155, v66 offset:52784
	ds_write_b32 v155, v67 offset:1584
	v_fma_f32 v66, -v62, v62, 1.0
	ds_read_b32 v67, v154 offset:128
	v_max_f32_e32 v66, 0, v66
	v_sqrt_f32_e32 v66, v66
	v_add_f32_e32 v59, 1.0, v59
	v_exp_f32_e32 v60, v60
	s_waitcnt lgkmcnt(0)
	v_mul_f32_e32 v58, v58, v67
	v_mul_f32_e32 v58, v66, v58
	ds_write_b32 v154, v62 offset:51328
	ds_write_b32 v154, v58 offset:128
	v_add_f32_e32 v58, v171, v63
	v_mul_f32_e32 v58, 0xbfb8aa3b, v58
	v_exp_f32_e32 v58, v58
	v_add_u32_e32 v67, 0x200, v156
	v_rcp_f32_e32 v62, v59
	v_add_f32_e32 v60, 1.0, v60
	v_add_f32_e32 v58, 1.0, v58
	v_rcp_f32_e32 v58, v58
	v_rcp_f32_e32 v60, v60
	v_add_f32_e32 v54, v177, v54
	v_mul_f32_e32 v54, 0xbfb8aa3b, v54
	v_mul_f32_e32 v58, v106, v58
	v_mul_f32_e32 v58, 0x3fb8aa3b, v58
	v_exp_f32_e32 v63, v58
	v_exp_f32_e32 v54, v54
	v_add_f32_e32 v55, v177, v55
	v_mul_f32_e32 v55, 0xbfb8aa3b, v55
	v_fma_f32 v58, -v63, v63, 1.0
	v_max_f32_e32 v58, 0, v58
	v_sqrt_f32_e32 v66, v58
	ds_read2_b32 v[58:59], v67 offset0:4 offset1:136
	v_add_f32_e32 v54, 1.0, v54
	v_rcp_f32_e32 v54, v54
	v_exp_f32_e32 v55, v55
	v_add_f32_e32 v50, v176, v50
	s_waitcnt lgkmcnt(0)
	v_mul_f32_e32 v58, v62, v58
	v_add_f32_e32 v62, v171, v64
	v_mul_f32_e32 v62, 0xbfb8aa3b, v62
	v_exp_f32_e32 v62, v62
	v_mul_f32_e32 v58, v66, v58
	v_mul_f32_e32 v59, v60, v59
	v_add_u32_e32 v60, 0xca00, v156
	v_add_f32_e32 v62, 1.0, v62
	v_rcp_f32_e32 v62, v62
	v_mul_f32_e32 v54, v107, v54
	v_mul_f32_e32 v54, 0x3fb8aa3b, v54
	v_exp_f32_e32 v54, v54
	v_mul_f32_e32 v62, v106, v62
	v_mul_f32_e32 v62, 0x3fb8aa3b, v62
	v_exp_f32_e32 v62, v62
	v_add_f32_e32 v55, 1.0, v55
	v_mul_f32_e32 v50, 0xbfb8aa3b, v50
	v_rcp_f32_e32 v55, v55
	v_fma_f32 v64, -v62, v62, 1.0
	v_max_f32_e32 v64, 0, v64
	v_sqrt_f32_e32 v64, v64
	v_exp_f32_e32 v50, v50
	v_add_f32_e32 v51, v176, v51
	v_mul_f32_e32 v55, v107, v55
	v_mul_f32_e32 v59, v64, v59
	ds_write2_b32 v60, v63, v62 offset0:4 offset1:136
	ds_write2_b32 v67, v58, v59 offset0:4 offset1:136
	v_add_f32_e32 v58, v171, v65
	v_mul_f32_e32 v58, 0xbfb8aa3b, v58
	v_exp_f32_e32 v58, v58
	v_add_f32_e32 v59, v175, v61
	v_mul_f32_e32 v59, 0xbfb8aa3b, v59
	v_exp_f32_e32 v59, v59
	v_add_f32_e32 v58, 1.0, v58
	v_rcp_f32_e32 v58, v58
	ds_read_b32 v61, v156 offset:1584
	v_add_f32_e32 v59, 1.0, v59
	v_rcp_f32_e32 v59, v59
	v_mul_f32_e32 v58, v106, v58
	v_mul_f32_e32 v58, 0x3fb8aa3b, v58
	v_exp_f32_e32 v58, v58
	s_waitcnt lgkmcnt(0)
; __device__ __forceinline__ float fexp_(float x) { return __builtin_amdgcn_exp2f(x * 1.4426950408889634f); }
; __device__ __forceinline__ float sigmoidf_(float x) { return __builtin_amdgcn_rcpf(1.0f + fexp_(-x)); }
; template <int MODE> ...
;     ...
;             for (int j = 0; j < 4; ++j) {
;                 const int col = (jt0 + j) * 16 + fr;
; #pragma unroll
;                 for (int r = 0; r < 4; ++r) {
;                     const int sl = st * 16 + fq * 4 + r;
;                     const float rg = sigmoidf_(ar[j][r] + bra[j]), ig = sigmoidf_(ai[j][r] + bri[j]);
;                     const float a = fexp_(rg * ls[j]);
;                     const float bv = __builtin_amdgcn_sqrtf(fmaxf(1.0f - a * a, 0.f)) * (ig * XC[sl * 132 + col]);
;                     AA[sl * 132 + col] = a; BB[sl * 132 + col] = bv;
;                 }
;             }
;         }
;         __syncthreads();
;         float ap = 1.f, he = 0.f;
; #pragma unroll
;         for (int q = 0; q < 16; ++q) { const float a = AA[(seg * 16 + q) * 132 + sj], bv = BB[(seg * 16 + q) * 132 + sj]; he = a * he + bv; ap *= a; }
;         SEG[seg * 128 + sj] = ap; SEG[512 + seg * 128 + sj] = he;
;         __syncthreads();
;         float hin = (MODE == 1) ? hin0 : 0.f;
; #pragma unroll
;         for (int s2 = 0; s2 < 3; ++s2) if (s2 < seg) hin = SEG[s2 * 128 + sj] * hin + SEG[512 + s2 * 128 + sj];
	v_mul_f32_e32 v59, v59, v61
	v_add_f32_e32 v50, 1.0, v50
	v_mul_f32_e32 v51, 0xbfb8aa3b, v51
	v_fma_f32 v60, -v58, v58, 1.0
	v_max_f32_e32 v60, 0, v60
	v_sqrt_f32_e32 v60, v60
	v_mul_f32_e32 v55, 0x3fb8aa3b, v55
	v_rcp_f32_e32 v50, v50
	v_exp_f32_e32 v51, v51
	v_mul_f32_e32 v59, v60, v59
	ds_write_b32 v156, v58 offset:52784
	ds_write_b32 v156, v59 offset:1584
	v_fma_f32 v58, -v54, v54, 1.0
	v_max_f32_e32 v58, 0, v58
	v_sqrt_f32_e32 v60, v58
	ds_read2_b32 v[58:59], v157 offset1:132
	v_exp_f32_e32 v55, v55
	v_add_f32_e32 v51, 1.0, v51
	v_rcp_f32_e32 v51, v51
	v_add_f32_e32 v53, v176, v53
	s_waitcnt lgkmcnt(0)
	v_mul_f32_e32 v50, v50, v58
	v_fma_f32 v58, -v55, v55, 1.0
	v_max_f32_e32 v58, 0, v58
	v_sqrt_f32_e32 v58, v58
	v_mul_f32_e32 v51, v51, v59
	v_mul_f32_e32 v50, v60, v50
	v_mul_f32_e32 v53, 0xbfb8aa3b, v53
	v_mul_f32_e32 v51, v58, v51
	v_add_u32_e32 v58, 0xc800, v157
	ds_write2_b32 v58, v54, v55 offset1:132
	ds_write2_b32 v157, v50, v51 offset1:132
	v_add_f32_e32 v50, v177, v56
	v_mul_f32_e32 v50, 0xbfb8aa3b, v50
	v_exp_f32_e32 v50, v50
	v_add_f32_e32 v51, v176, v52
	v_mul_f32_e32 v51, 0xbfb8aa3b, v51
	v_exp_f32_e32 v51, v51
	v_add_f32_e32 v50, 1.0, v50
	v_rcp_f32_e32 v50, v50
	v_add_u32_e32 v56, 0x400, v157
	v_add_f32_e32 v51, 1.0, v51
	v_rcp_f32_e32 v52, v51
	v_mul_f32_e32 v50, v107, v50
	v_mul_f32_e32 v50, 0x3fb8aa3b, v50
	v_exp_f32_e32 v54, v50
	v_exp_f32_e32 v53, v53
	v_add_u32_e32 v66, 0xc800, v158
	v_add_u32_e32 v64, 0xcc00, v158
	v_fma_f32 v50, -v54, v54, 1.0
	v_max_f32_e32 v50, 0, v50
	v_sqrt_f32_e32 v55, v50
	ds_read2_b32 v[50:51], v56 offset0:8 offset1:140
	v_add_f32_e32 v53, 1.0, v53
	v_rcp_f32_e32 v53, v53
	v_add_u32_e32 v65, 0x400, v158
	v_add_u32_e32 v62, 0xd000, v158
	s_waitcnt lgkmcnt(0)
	v_mul_f32_e32 v50, v52, v50
	v_add_f32_e32 v52, v177, v57
	v_mul_f32_e32 v52, 0xbfb8aa3b, v52
	v_exp_f32_e32 v52, v52
	v_mul_f32_e32 v50, v55, v50
	v_mul_f32_e32 v51, v53, v51
	v_add_u32_e32 v53, 0xcc00, v157
	v_add_f32_e32 v52, 1.0, v52
	v_rcp_f32_e32 v52, v52
	v_add_u32_e32 v63, 0x800, v158
	v_add_u32_e32 v60, 0xd400, v158
	v_add_u32_e32 v61, 0xc00, v158
	v_mul_f32_e32 v52, v107, v52
	v_mul_f32_e32 v52, 0x3fb8aa3b, v52
	v_exp_f32_e32 v52, v52
	v_add_u32_e32 v58, 0xd800, v158
	v_add_u32_e32 v59, 0x1000, v158
	v_add_u32_e32 v57, 0x1400, v158
	v_fma_f32 v55, -v52, v52, 1.0
	v_max_f32_e32 v55, 0, v55
	v_sqrt_f32_e32 v55, v55
	s_nop 0
	v_mul_f32_e32 v51, v55, v51
	ds_write2_b32 v53, v54, v52 offset0:8 offset1:140
	ds_write2_b32 v56, v50, v51 offset0:8 offset1:140
	s_waitcnt lgkmcnt(0)
	s_barrier
	v_add_u32_e32 v56, 0xdc00, v158
	v_add_u32_e32 v54, 0xe000, v158
	v_add_u32_e32 v55, 0x1800, v158
	v_add_u32_e32 v52, 0xe400, v158
	v_add_u32_e32 v53, 0x1c00, v158
	ds_read2_b32 v[222:223], v66 offset1:132
	ds_read2_b32 v[238:239], v158 offset1:132
	ds_read2_b32 v[224:225], v64 offset0:8 offset1:140
	ds_read2_b32 v[240:241], v65 offset0:8 offset1:140
	ds_read2_b32 v[226:227], v62 offset0:16 offset1:148
	ds_read2_b32 v[244:245], v63 offset0:16 offset1:148
	ds_read2_b32 v[228:229], v60 offset0:24 offset1:156
	ds_read2_b32 v[246:247], v61 offset0:24 offset1:156
	ds_read2_b32 v[230:231], v58 offset0:32 offset1:164
	ds_read2_b32 v[248:249], v59 offset0:32 offset1:164
	ds_read2_b32 v[232:233], v56 offset0:40 offset1:172
	ds_read2_b32 v[250:251], v57 offset0:40 offset1:172
	ds_read2_b32 v[234:235], v54 offset0:48 offset1:180
	ds_read2_b32 v[252:253], v55 offset0:48 offset1:180
	ds_read2_b32 v[236:237], v52 offset0:56 offset1:188
	ds_read2_b32 v[254:255], v53 offset0:56 offset1:188
	s_waitcnt lgkmcnt(14)
	v_fma_f32 v51, 0, v222, v238
	v_fma_f32 v51, v51, v223, v239
	v_mul_f32_e32 v67, v222, v223
	s_waitcnt lgkmcnt(12)
	v_fma_f32 v51, v51, v224, v240
	v_mul_f32_e32 v67, v67, v224
	v_fma_f32 v51, v51, v225, v241
	v_mul_f32_e32 v67, v67, v225
	s_waitcnt lgkmcnt(10)
	v_fma_f32 v51, v51, v226, v244
	v_mul_f32_e32 v67, v67, v226
	v_fma_f32 v51, v51, v227, v245
	v_mul_f32_e32 v67, v67, v227
	s_waitcnt lgkmcnt(8)
	v_fma_f32 v51, v51, v228, v246
	v_mul_f32_e32 v67, v67, v228
	v_fma_f32 v51, v51, v229, v247
	v_mul_f32_e32 v67, v67, v229
	s_waitcnt lgkmcnt(6)
	v_fma_f32 v51, v51, v230, v248
	v_mul_f32_e32 v67, v67, v230
	v_fma_f32 v51, v51, v231, v249
	v_mul_f32_e32 v67, v67, v231
	s_waitcnt lgkmcnt(4)
	v_fma_f32 v51, v51, v232, v250
	v_mul_f32_e32 v67, v67, v232
	v_fma_f32 v51, v51, v233, v251
	v_mul_f32_e32 v67, v67, v233
	s_waitcnt lgkmcnt(2)
	v_fma_f32 v51, v51, v234, v252
	v_mul_f32_e32 v67, v67, v234
	v_fma_f32 v51, v51, v235, v253
	v_mul_f32_e32 v67, v67, v235
	s_waitcnt lgkmcnt(0)
	v_fma_f32 v51, v51, v236, v254
	v_mul_f32_e32 v67, v67, v236
	v_fma_f32 v51, v51, v237, v255
	v_mul_f32_e32 v67, v67, v237
	v_mov_b32_e32 v50, 0
	ds_write2st64_b32 v113, v67, v51 offset1:8
	s_waitcnt lgkmcnt(0)
	s_barrier
	s_and_saveexec_b64 s[6:7], s[42:43]
	s_cbranch_execnz .LBB0_271
	s_or_b64 exec, exec, s[6:7]
	s_and_saveexec_b64 s[6:7], s[44:45]
	s_cbranch_execnz .LBB0_272

; __device__ __forceinline__ unsigned pk2(float lo, float hi) { const f32x2c_t v = {lo, hi}; const bf16x2c_t b = __builtin_convertvector(v, bf16x2c_t); return __builtin_bit_cast(unsigned, b); }
; __device__ __forceinline__ float bflo(unsigned w) { return __uint_as_float(w << 16); }
; __device__ __forceinline__ float bfhi(unsigned w) { return __uint_as_float(w & 0xffff0000u); }
; __device__ __forceinline__ float gelu_tanh(float x) { const float y = 0.7978845608028654f * (x + 0.044715f * x * x * x); return x * __builtin_amdgcn_rcpf(1.0f + fexp_(-2.0f * y)); }
; template <int MODE> ...
;     ...
;             float acum = 1.f;
; #pragma unroll
;             for (int s2 = 0; s2 < 3; ++s2) if (s2 < seg) acum *= SEG[s2 * 128 + sj];
;             float hcur = hin;
; #pragma unroll
;             for (int q = 0; q < 16; ++q) { const int o = (seg * 16 + q) * 132 + sj; const float a = AA[o]; hcur = a * hcur + BB[o]; acum *= a; BB[o] = hcur; AA[o] = acum; }
;             __syncthreads();
;             const unsigned gw[8] = {gc0.x, gc0.y, gc0.z, gc0.w, gc1.x, gc1.y, gc1.z, gc1.w};
;             unsigned oy[8], ow[8];
; #pragma unroll
;             for (int q = 0; q < 8; ++q) { const float g0 = gelu_tanh(bflo(gw[q])), g1 = gelu_tanh(bfhi(gw[q]));
;                 oy[q] = pk2(BB[m * 132 + j0 + 2 * q] * g0, BB[m * 132 + j0 + 2 * q + 1] * g1);
;                 ow[q] = pk2(AA[m * 132 + j0 + 2 * q] * g0, AA[m * 132 + j0 + 2 * q + 1] * g1); }
.LBB0_269:
	s_or_b64 exec, exec, s[6:7]
	v_fma_f32 v238, v50, v222, v238
	v_fmac_f32_e32 v239, v238, v223
	v_mul_f32_e32 v222, v51, v222
	v_mul_f32_e32 v223, v222, v223
	ds_write2_b32 v158, v238, v239 offset1:132
	ds_write2_b32 v66, v222, v223 offset1:132
	v_fma_f32 v240, v239, v224, v240
	v_fmac_f32_e32 v241, v240, v225
	v_mul_f32_e32 v224, v223, v224
	v_mul_f32_e32 v225, v224, v225
	ds_write2_b32 v65, v240, v241 offset0:8 offset1:140
	ds_write2_b32 v64, v224, v225 offset0:8 offset1:140
	v_fma_f32 v244, v241, v226, v244
	v_fmac_f32_e32 v245, v244, v227
	v_mul_f32_e32 v226, v225, v226
	v_mul_f32_e32 v227, v226, v227
	ds_write2_b32 v63, v244, v245 offset0:16 offset1:148
	ds_write2_b32 v62, v226, v227 offset0:16 offset1:148
	v_fma_f32 v246, v245, v228, v246
	v_fmac_f32_e32 v247, v246, v229
	v_mul_f32_e32 v228, v227, v228
	v_mul_f32_e32 v229, v228, v229
	ds_write2_b32 v61, v246, v247 offset0:24 offset1:156
	ds_write2_b32 v60, v228, v229 offset0:24 offset1:156
	v_fma_f32 v248, v247, v230, v248
	v_fmac_f32_e32 v249, v248, v231
	v_mul_f32_e32 v230, v229, v230
	v_mul_f32_e32 v231, v230, v231
	ds_write2_b32 v59, v248, v249 offset0:32 offset1:164
	ds_write2_b32 v58, v230, v231 offset0:32 offset1:164
	v_fma_f32 v250, v249, v232, v250
	v_fmac_f32_e32 v251, v250, v233
	v_mul_f32_e32 v232, v231, v232
	v_mul_f32_e32 v233, v232, v233
	ds_write2_b32 v57, v250, v251 offset0:40 offset1:172
	ds_write2_b32 v56, v232, v233 offset0:40 offset1:172
	v_fma_f32 v252, v251, v234, v252
	v_fmac_f32_e32 v253, v252, v235
	v_mul_f32_e32 v234, v233, v234
	v_mul_f32_e32 v235, v234, v235
	ds_write2_b32 v55, v252, v253 offset0:48 offset1:180
	ds_write2_b32 v54, v234, v235 offset0:48 offset1:180
	v_fma_f32 v254, v253, v236, v254
	v_fmac_f32_e32 v255, v254, v237
	v_mul_f32_e32 v236, v235, v236
	v_mul_f32_e32 v237, v236, v237
	ds_write2_b32 v53, v254, v255 offset0:56 offset1:188
	ds_write2_b32 v52, v236, v237 offset0:56 offset1:188
	s_waitcnt lgkmcnt(0)
	s_barrier
	s_mov_b32 s98, 0xbdd2d3e7
	s_mov_b32 s99, 0xc0135761
	ds_read_b128 v[50:53], v164
	ds_read_b128 v[222:225], v164 offset:51200
	ds_read_b128 v[54:57], v164 offset:16
	ds_read_b128 v[226:229], v164 offset:51216
	ds_read_b128 v[58:61], v164 offset:32
	ds_read_b128 v[230:233], v164 offset:51232
	ds_read_b128 v[62:65], v164 offset:48
	ds_read_b128 v[234:237], v164 offset:51248
	v_lshlrev_b32_e32 v238, 16, v6
	v_lshlrev_b32_e32 v240, 16, v7
	v_and_b32_e32 v239, 0xffff0000, v6
	v_and_b32_e32 v241, 0xffff0000, v7
	v_pk_mul_f32 v[66:67], v[238:239], v[238:239]
	v_pk_mul_f32 v[68:69], v[240:241], v[240:241]
	v_pk_fma_f32 v[66:67], v[66:67], s[98:99], s[98:99] op_sel:[0,0,1] op_sel_hi:[1,0,1]
	v_pk_fma_f32 v[68:69], v[68:69], s[98:99], s[98:99] op_sel:[0,0,1] op_sel_hi:[1,0,1]
	v_pk_mul_f32 v[66:67], v[66:67], v[238:239]
	v_pk_mul_f32 v[68:69], v[68:69], v[240:241]
	v_exp_f32_e32 v66, v66
	v_exp_f32_e32 v67, v67
	v_exp_f32_e32 v68, v68
	v_exp_f32_e32 v69, v69
	v_pk_add_f32 v[66:67], v[66:67], 1.0 op_sel_hi:[1,0]
	v_pk_add_f32 v[68:69], v[68:69], 1.0 op_sel_hi:[1,0]
	v_rcp_f32_e32 v66, v66
	v_rcp_f32_e32 v67, v67
	v_rcp_f32_e32 v68, v68
	v_rcp_f32_e32 v69, v69
	v_pk_mul_f32 v[238:239], v[66:67], v[238:239]
	v_pk_mul_f32 v[240:241], v[68:69], v[240:241]
	v_lshlrev_b32_e32 v244, 16, v8
	v_lshlrev_b32_e32 v246, 16, v9
	v_and_b32_e32 v245, 0xffff0000, v8
	v_and_b32_e32 v247, 0xffff0000, v9
	v_pk_mul_f32 v[66:67], v[244:245], v[244:245]
	v_pk_mul_f32 v[68:69], v[246:247], v[246:247]
	v_pk_fma_f32 v[66:67], v[66:67], s[98:99], s[98:99] op_sel:[0,0,1] op_sel_hi:[1,0,1]
	v_pk_fma_f32 v[68:69], v[68:69], s[98:99], s[98:99] op_sel:[0,0,1] op_sel_hi:[1,0,1]
	v_pk_mul_f32 v[66:67], v[66:67], v[244:245]
	v_pk_mul_f32 v[68:69], v[68:69], v[246:247]
	v_exp_f32_e32 v66, v66
	v_exp_f32_e32 v67, v67
	v_exp_f32_e32 v68, v68
	v_exp_f32_e32 v69, v69
	v_pk_add_f32 v[66:67], v[66:67], 1.0 op_sel_hi:[1,0]
	v_pk_add_f32 v[68:69], v[68:69], 1.0 op_sel_hi:[1,0]
	v_rcp_f32_e32 v66, v66
	v_rcp_f32_e32 v67, v67
	v_rcp_f32_e32 v68, v68
	v_rcp_f32_e32 v69, v69
	v_pk_mul_f32 v[244:245], v[66:67], v[244:245]
	v_pk_mul_f32 v[246:247], v[68:69], v[246:247]
	v_lshlrev_b32_e32 v248, 16, v2
	v_lshlrev_b32_e32 v250, 16, v3
	v_and_b32_e32 v249, 0xffff0000, v2
	v_and_b32_e32 v251, 0xffff0000, v3
	v_pk_mul_f32 v[66:67], v[248:249], v[248:249]
	v_pk_mul_f32 v[68:69], v[250:251], v[250:251]
	v_pk_fma_f32 v[66:67], v[66:67], s[98:99], s[98:99] op_sel:[0,0,1] op_sel_hi:[1,0,1]
	v_pk_fma_f32 v[68:69], v[68:69], s[98:99], s[98:99] op_sel:[0,0,1] op_sel_hi:[1,0,1]
	v_pk_mul_f32 v[66:67], v[66:67], v[248:249]
	v_pk_mul_f32 v[68:69], v[68:69], v[250:251]
	v_exp_f32_e32 v66, v66
	v_exp_f32_e32 v67, v67
	v_exp_f32_e32 v68, v68
	v_exp_f32_e32 v69, v69
	v_pk_add_f32 v[66:67], v[66:67], 1.0 op_sel_hi:[1,0]
	v_pk_add_f32 v[68:69], v[68:69], 1.0 op_sel_hi:[1,0]
	v_rcp_f32_e32 v66, v66
	v_rcp_f32_e32 v67, v67
	v_rcp_f32_e32 v68, v68
	v_rcp_f32_e32 v69, v69
	v_pk_mul_f32 v[248:249], v[66:67], v[248:249]
	v_pk_mul_f32 v[250:251], v[68:69], v[250:251]
	v_lshlrev_b32_e32 v252, 16, v4
	v_lshlrev_b32_e32 v254, 16, v5
	v_and_b32_e32 v253, 0xffff0000, v4
	v_and_b32_e32 v255, 0xffff0000, v5
	v_pk_mul_f32 v[66:67], v[252:253], v[252:253]
	v_pk_mul_f32 v[68:69], v[254:255], v[254:255]
	v_pk_fma_f32 v[66:67], v[66:67], s[98:99], s[98:99] op_sel:[0,0,1] op_sel_hi:[1,0,1]
	v_pk_fma_f32 v[68:69], v[68:69], s[98:99], s[98:99] op_sel:[0,0,1] op_sel_hi:[1,0,1]
	v_pk_mul_f32 v[66:67], v[66:67], v[252:253]
	v_pk_mul_f32 v[68:69], v[68:69], v[254:255]
	v_exp_f32_e32 v66, v66
	v_exp_f32_e32 v67, v67
	v_exp_f32_e32 v68, v68
	v_exp_f32_e32 v69, v69
	v_pk_add_f32 v[66:67], v[66:67], 1.0 op_sel_hi:[1,0]
	v_pk_add_f32 v[68:69], v[68:69], 1.0 op_sel_hi:[1,0]
	v_rcp_f32_e32 v66, v66
	v_rcp_f32_e32 v67, v67
	v_rcp_f32_e32 v68, v68
	v_rcp_f32_e32 v69, v69
	v_pk_mul_f32 v[252:253], v[66:67], v[252:253]
	v_pk_mul_f32 v[254:255], v[68:69], v[254:255]
	s_waitcnt lgkmcnt(0)
; __device__ __forceinline__ unsigned pk2(float lo, float hi) { const f32x2c_t v = {lo, hi}; const bf16x2c_t b = __builtin_convertvector(v, bf16x2c_t); return __builtin_bit_cast(unsigned, b); }
; __device__ __forceinline__ float bflo(unsigned w) { return __uint_as_float(w << 16); }
; __device__ __forceinline__ float bfhi(unsigned w) { return __uint_as_float(w & 0xffff0000u); }
; __device__ __forceinline__ float gelu_tanh(float x) { const float y = 0.7978845608028654f * (x + 0.044715f * x * x * x); return x * __builtin_amdgcn_rcpf(1.0f + fexp_(-2.0f * y)); }
; template <int ISV>
; __device__ __forceinline__ void quant_finish(const QRow& q, unsigned char* qtab, float* scales, int e, int lane) {
;     float amax = 0.f;
; #pragma unroll
;     for (int j = 0; j < 8; ++j) amax = fmaxf(amax, fmaxf(fmaxf(fabsf(q.v[j].x), fabsf(q.v[j].y)), fmaxf(fabsf(q.v[j].z), fabsf(q.v[j].w))));
;     amax = wave_max(amax);
;     unsigned* qp = (unsigned*)qtab + (size_t)e * 64;
;     {
;         const float inv = amax > 0.f ? 127.0f / amax : 0.f;
;         if (lane == 0) scales[e] = amax * (1.0f / 127.0f);
; template <int MODE> ...
;     ...
;             const unsigned gw[8] = {gc0.x, gc0.y, gc0.z, gc0.w, gc1.x, gc1.y, gc1.z, gc1.w};
;             unsigned oy[8], ow[8];
; #pragma unroll
;             for (int q = 0; q < 8; ++q) { const float g0 = gelu_tanh(bflo(gw[q])), g1 = gelu_tanh(bfhi(gw[q]));
;                 oy[q] = pk2(BB[m * 132 + j0 + 2 * q] * g0, BB[m * 132 + j0 + 2 * q + 1] * g1);
;                 ow[q] = pk2(AA[m * 132 + j0 + 2 * q] * g0, AA[m * 132 + j0 + 2 * q + 1] * g1); }
;             const size_t yo = (size_t)(n * 64 + m) * 1024 + c0 + j0;
;             *(u32x4*)(Y0 + yo) = (u32x4){oy[0], oy[1], oy[2], oy[3]}; *(u32x4*)(Y0 + yo + 8) = (u32x4){oy[4], oy[5], oy[6], oy[7]};
;             *(u32x4*)(W0 + yo) = (u32x4){ow[0], ow[1], ow[2], ow[3]}; *(u32x4*)(W0 + yo + 8) = (u32x4){ow[4], ow[5], ow[6], ow[7]};
	v_pk_mul_f32 v[66:67], v[238:239], v[50:51]
	v_pk_mul_f32 v[238:239], v[238:239], v[222:223]
	v_cvt_pk_bf16_f32 v50, v66, v67
	v_cvt_pk_bf16_f32 v6, v238, v239
	v_pk_mul_f32 v[68:69], v[240:241], v[52:53]
	v_pk_mul_f32 v[240:241], v[240:241], v[224:225]
	v_cvt_pk_bf16_f32 v51, v68, v69
	v_cvt_pk_bf16_f32 v7, v240, v241
	v_pk_mul_f32 v[66:67], v[244:245], v[54:55]
	v_pk_mul_f32 v[244:245], v[244:245], v[226:227]
	v_cvt_pk_bf16_f32 v52, v66, v67
	v_cvt_pk_bf16_f32 v8, v244, v245
	v_pk_mul_f32 v[68:69], v[246:247], v[56:57]
	v_pk_mul_f32 v[246:247], v[246:247], v[228:229]
	v_cvt_pk_bf16_f32 v53, v68, v69
	v_cvt_pk_bf16_f32 v9, v246, v247
	v_pk_mul_f32 v[66:67], v[248:249], v[58:59]
	v_pk_mul_f32 v[248:249], v[248:249], v[230:231]
	v_cvt_pk_bf16_f32 v54, v66, v67
	v_cvt_pk_bf16_f32 v2, v248, v249
	v_pk_mul_f32 v[68:69], v[250:251], v[60:61]
	v_pk_mul_f32 v[250:251], v[250:251], v[232:233]
	v_cvt_pk_bf16_f32 v55, v68, v69
	v_cvt_pk_bf16_f32 v3, v250, v251
	v_pk_mul_f32 v[66:67], v[252:253], v[62:63]
	v_pk_mul_f32 v[252:253], v[252:253], v[234:235]
	v_cvt_pk_bf16_f32 v56, v66, v67
	v_cvt_pk_bf16_f32 v4, v252, v253
	v_pk_mul_f32 v[68:69], v[254:255], v[64:65]
	v_pk_mul_f32 v[254:255], v[254:255], v[236:237]
	v_cvt_pk_bf16_f32 v57, v68, v69
	v_cvt_pk_bf16_f32 v5, v254, v255
	v_lshl_add_u32 v58, s0, 6, v79
	v_ashrrev_i32_e32 v59, 31, v58
	v_lshlrev_b64 v[58:59], 10, v[58:59]
	v_or_b32_e32 v58, s18, v58
	v_or_b32_e32 v58, v58, v78
	v_lshlrev_b64 v[58:59], 1, v[58:59]
	v_lshl_add_u64 v[60:61], s[72:73], 0, v[58:59]
	v_lshl_add_u64 v[62:63], s[90:91], 0, v[58:59]
	global_store_dwordx4 v[60:61], v[50:53], off
	global_store_dwordx4 v[60:61], v[54:57], off offset:16
	global_store_dwordx4 v[62:63], v[6:9], off
	global_store_dwordx4 v[62:63], v[2:5], off offset:16
	s_waitcnt vmcnt(11)
	s_nop 0
	v_max_f32_e64 v2, |v49|, |v49|
	v_max_f32_e64 v3, |v48|, |v48|
	v_max_f32_e32 v2, v3, v2
	s_waitcnt vmcnt(10)
	v_max_f32_e64 v3, |v45|, |v45|
	v_max_f32_e64 v4, |v44|, |v44|
	v_max_f32_e32 v3, v4, v3
	v_max3_f32 v2, |v46|, |v47|, v2
	v_max3_f32 v3, |v42|, |v43|, v3
	v_max3_f32 v2, v2, 0, v3
	s_waitcnt vmcnt(9)
	v_max_f32_e64 v3, |v41|, |v41|
	v_max_f32_e64 v4, |v40|, |v40|
	v_max_f32_e32 v3, v4, v3
	s_waitcnt vmcnt(8)
	v_max_f32_e64 v4, |v37|, |v37|
	v_max_f32_e64 v5, |v36|, |v36|
	v_max_f32_e32 v4, v5, v4
	v_max3_f32 v3, |v38|, |v39|, v3
	v_max3_f32 v4, |v34|, |v35|, v4
	v_max3_f32 v2, v2, v3, v4
	s_waitcnt vmcnt(7)
	v_max_f32_e64 v3, |v33|, |v33|
	v_max_f32_e64 v4, |v32|, |v32|
	v_max_f32_e32 v3, v4, v3
	s_waitcnt vmcnt(6)
	v_max_f32_e64 v4, |v29|, |v29|
	v_max_f32_e64 v5, |v28|, |v28|
	v_max_f32_e32 v4, v5, v4
	v_max3_f32 v3, |v30|, |v31|, v3
	v_max3_f32 v4, |v26|, |v27|, v4
	v_max3_f32 v2, v2, v3, v4
	s_waitcnt vmcnt(5)
	v_max_f32_e64 v3, |v25|, |v25|
	v_max_f32_e64 v4, |v24|, |v24|
	v_max_f32_e32 v3, v4, v3
	s_waitcnt vmcnt(4)
	v_max_f32_e64 v4, |v21|, |v21|
	v_max_f32_e64 v5, |v20|, |v20|
	v_max_f32_e32 v4, v5, v4
	v_max3_f32 v3, |v22|, |v23|, v3
	v_max3_f32 v4, |v18|, |v19|, v4
	v_max3_f32 v2, v2, v3, v4
	ds_bpermute_b32 v3, v114, v2
	s_waitcnt lgkmcnt(0)
	v_max_f32_e32 v3, v3, v3
	v_max_f32_e32 v2, v2, v3
	ds_bpermute_b32 v3, v115, v2
	s_waitcnt lgkmcnt(0)
	v_max_f32_e32 v3, v3, v3
	v_max_f32_e32 v2, v2, v3
	ds_bpermute_b32 v3, v116, v2
	s_waitcnt lgkmcnt(0)
	v_max_f32_e32 v3, v3, v3
	v_max_f32_e32 v2, v2, v3
	ds_bpermute_b32 v3, v117, v2
	s_waitcnt lgkmcnt(0)
	v_max_f32_e32 v3, v3, v3
	v_max_f32_e32 v2, v2, v3
	ds_bpermute_b32 v3, v118, v2
	s_waitcnt lgkmcnt(0)
	v_max_f32_e32 v3, v3, v3
	v_max_f32_e32 v2, v2, v3
	ds_bpermute_b32 v3, v119, v2
	s_waitcnt lgkmcnt(0)
	v_max_f32_e32 v3, v3, v3
	v_max_f32_e32 v2, v2, v3
	s_and_saveexec_b64 s[6:7], s[40:41]
	s_cbranch_execz .LBB0_240
	s_lshl_b64 s[22:23], s[48:49], 2
	s_add_u32 s22, s86, s22
	s_addc_u32 s23, s87, s23
	v_mul_f32_e32 v3, 0x3c010204, v2
	global_store_dword v85, v3, s[22:23]
	s_branch .LBB0_240

; __global__ void __launch_bounds__(NTHREADS, 2) mega_fwd(Ptrs P) {
	.amdhsa_kernel _Z8mega_fwd4Ptrs
		.amdhsa_group_segment_fixed_size 0
		.amdhsa_private_segment_fixed_size 0
		.amdhsa_kernarg_size 424
		.amdhsa_user_sgpr_count 2
		.amdhsa_user_sgpr_dispatch_ptr 0
		.amdhsa_user_sgpr_queue_ptr 0
		.amdhsa_user_sgpr_kernarg_segment_ptr 1
		.amdhsa_user_sgpr_dispatch_id 0
		.amdhsa_user_sgpr_kernarg_preload_length 0
		.amdhsa_user_sgpr_kernarg_preload_offset 0
		.amdhsa_user_sgpr_private_segment_size 0
		.amdhsa_uses_dynamic_stack 0
		.amdhsa_enable_private_segment 0
		.amdhsa_system_sgpr_workgroup_id_x 1
		.amdhsa_system_sgpr_workgroup_id_y 0
		.amdhsa_system_sgpr_workgroup_id_z 0
		.amdhsa_system_sgpr_workgroup_info 0
		.amdhsa_system_vgpr_workitem_id 0
		.amdhsa_next_free_vgpr 256
		.amdhsa_next_free_sgpr 102
		.amdhsa_accum_offset 256
		.amdhsa_reserve_vcc 1
		.amdhsa_float_round_mode_32 0
		.amdhsa_float_round_mode_16_64 0
		.amdhsa_float_denorm_mode_32 3
		.amdhsa_float_denorm_mode_16_64 3
		.amdhsa_dx10_clamp 1
		.amdhsa_ieee_mode 1
		.amdhsa_fp16_overflow 0
		.amdhsa_tg_split 0
		.amdhsa_exception_fp_ieee_invalid_op 0
		.amdhsa_exception_fp_denorm_src 0
		.amdhsa_exception_fp_ieee_div_zero 0
		.amdhsa_exception_fp_ieee_overflow 0
		.amdhsa_exception_fp_ieee_underflow 0
		.amdhsa_exception_fp_ieee_inexact 0
		.amdhsa_exception_int_div_zero 0
	.end_amdhsa_kernel

; __global__ void __launch_bounds__(NTHREADS, 2) mega_fwd(Ptrs P) {
amdhsa.kernels:
  - .agpr_count:     0
    .args:
      - .offset:         0
        .size:           168
        .value_kind:     by_value
      - .offset:         168
        .size:           4
        .value_kind:     hidden_block_count_x
      - .offset:         172
        .size:           4
        .value_kind:     hidden_block_count_y
      - .offset:         176
        .size:           4
        .value_kind:     hidden_block_count_z
      - .offset:         180
        .size:           2
        .value_kind:     hidden_group_size_x
      - .offset:         182
        .size:           2
        .value_kind:     hidden_group_size_y
      - .offset:         184
        .size:           2
        .value_kind:     hidden_group_size_z
      - .offset:         186
        .size:           2
        .value_kind:     hidden_remainder_x
      - .offset:         188
        .size:           2
        .value_kind:     hidden_remainder_y
      - .offset:         190
        .size:           2
        .value_kind:     hidden_remainder_z
      - .offset:         208
        .size:           8
        .value_kind:     hidden_global_offset_x
      - .offset:         216
        .size:           8
        .value_kind:     hidden_global_offset_y
      - .offset:         224
        .size:           8
        .value_kind:     hidden_global_offset_z
      - .offset:         232
        .size:           2
        .value_kind:     hidden_grid_dims
      - .offset:         288
        .size:           4
        .value_kind:     hidden_dynamic_lds_size
    .group_segment_fixed_size: 0
    .kernarg_segment_align: 8
    .kernarg_segment_size: 424
    .language:       OpenCL C
    .language_version:
      - 2
      - 0
    .max_flat_workgroup_size: 512
    .name:           _Z8mega_fwd4Ptrs
    .private_segment_fixed_size: 0
    .sgpr_count:     108
    .sgpr_spill_count: 95
    .symbol:         _Z8mega_fwd4Ptrs.kd
    .uniform_work_group_size: 1
    .uses_dynamic_stack: false
    .vgpr_count:     256
    .vgpr_spill_count: 0
    .wavefront_size: 64
